# speedup vs baseline: 1.0090x; 1.0090x over previous
.LBB0_2:
	s_andn2_b64 vcc, exec, s[6:7]
	s_cbranch_vccnz .LBB0_66
	v_bfe_u32 v1, v0, 5, 1
	v_lshrrev_b32_e32 v2, 1, v0
	v_lshlrev_b32_e32 v4, 7, v0
	v_bfe_u32 v3, v0, 1, 3
	v_and_b32_e32 v4, 0xf80, v4
	v_bitop3_b32 v2, v1, v2, 7 bitop3:0x78
	v_lshl_or_b32 v230, v2, 4, v4
	v_bitop3_b32 v2, v1, v3, 2 bitop3:0x36
	v_lshl_or_b32 v231, v2, 4, v4
	v_bitop3_b32 v2, v1, v3, 4 bitop3:0x36
	v_lshl_or_b32 v232, v2, 4, v4
	v_bitop3_b32 v2, v1, v3, 6 bitop3:0x36
	v_lshlrev_b32_e32 v18, 4, v0
	s_load_dwordx2 s[72:73], s[0:1], 0x20
	s_load_dwordx4 s[68:71], s[0:1], 0x0
	s_load_dwordx2 s[74:75], s[0:1], 0x10
	v_lshl_or_b32 v233, v2, 4, v4
	v_lshlrev_b32_e32 v2, 1, v0
	v_lshlrev_b32_e32 v3, 3, v0
	v_and_b32_e32 v4, 0xc0, v18
	v_and_b32_e32 v2, 32, v2
	v_and_b32_e32 v3, 24, v3
	v_lshl_or_b32 v1, v1, 8, v4
	v_or3_b32 v234, v1, v2, v3
	v_mov_b32_e32 v3, 0
	s_lshr_b32 s6, s8, 6
	v_mov_b32_e32 v1, v3
	v_mov_b32_e32 v16, v3
	v_mov_b32_e32 v17, v3
	v_lshl_add_u64 v[226:227], s[4:5], 0, v[0:1]
	s_lshl_b32 s33, s6, 5
	s_waitcnt lgkmcnt(0)
	v_cmp_gt_u32_e64 s[34:35], 8, v0
	s_and_saveexec_b64 s[36:37], s[34:35]
	s_cbranch_execz .Lst_ub
	global_load_ubyte v162, v[226:227], off
.Lst_ub:
	s_or_b64 exec, exec, s[36:37]
	s_lshl_b32 s44, s76, 12
	s_lshl_b32 s45, s91, 8
	s_add_u32 s44, s44, s45
	s_add_u32 s34, s70, s44
	s_addc_u32 s35, s71, 0
	s_add_u32 s36, s74, s44
	s_addc_u32 s37, s75, 0
	s_add_u32 s38, s68, s44
	s_addc_u32 s39, s69, 0
	s_add_i32 s40, s3, -1
	s_cmp_gt_i32 s82, 1
	s_cselect_b32 s41, 64, 0
	s_add_i32 s42, s82, -1
	s_min_i32 s42, s42, 2
	s_lshl_b32 s42, s42, 6
	s_add_i32 s43, s89, s33
	v_lshrrev_b32_e32 v210, 4, v0
	v_and_b32_e32 v211, 15, v0
	v_lshlrev_b32_e32 v211, 4, v211
	v_bfe_u32 v214, v0, 4, 2
	v_add_u32_e32 v214, s43, v214
	v_min_i32_e32 v212, s40, v210
	v_lshl_add_u32 v212, v212, 12, v211
	global_load_dwordx4 v[70:73], v212, s[34:35]
	v_add_u32_e32 v213, 32, v210
	v_min_i32_e32 v213, s40, v213
	v_lshl_add_u32 v213, v213, 12, v211
	global_load_dwordx4 v[66:69], v213, s[34:35]
	global_load_dwordx4 v[182:185], v212, s[36:37]
	global_load_dwordx4 v[186:189], v213, s[36:37]
	v_add_u32_e32 v212, s41, v210
	v_min_i32_e32 v212, s40, v212
	v_lshl_add_u32 v212, v212, 12, v211
	global_load_dwordx4 v[90:93], v212, s[34:35]
	v_add3_u32 v213, s41, v210, 32
	v_min_i32_e32 v213, s40, v213
	v_lshl_add_u32 v213, v213, 12, v211
	global_load_dwordx4 v[82:85], v213, s[34:35]
	v_add_u32_e32 v212, s42, v210
	v_min_i32_e32 v212, s40, v212
	v_lshl_add_u32 v212, v212, 12, v211
	global_load_dwordx4 v[98:101], v212, s[34:35]
	v_add3_u32 v213, s42, v210, 32
	v_min_i32_e32 v213, s40, v213
	v_lshl_add_u32 v213, v213, 12, v211
	global_load_dwordx4 v[94:97], v213, s[34:35]
	v_min_i32_e32 v212, s40, v214
	v_lshl_add_u32 v212, v212, 12, v211
	global_load_dwordx4 v[86:89], v212, s[38:39] sc0 sc1 nt
	v_add_u32_e32 v213, 4, v214
	v_min_i32_e32 v213, s40, v213
	v_lshl_add_u32 v213, v213, 12, v211
	global_load_dwordx4 v[74:77], v213, s[38:39] sc0 sc1 nt
	v_add_u32_e32 v212, 8, v214
	v_min_i32_e32 v212, s40, v212
	v_lshl_add_u32 v212, v212, 12, v211
	global_load_dwordx4 v[78:81], v212, s[38:39] sc0 sc1 nt
	v_add_u32_e32 v213, 12, v214
	v_min_i32_e32 v213, s40, v213
	v_lshl_add_u32 v213, v213, 12, v211
	global_load_dwordx4 v[58:61], v213, s[38:39] sc0 sc1 nt
	v_add_u32_e32 v212, 16, v214
	v_min_i32_e32 v212, s40, v212
	v_lshl_add_u32 v212, v212, 12, v211
	global_load_dwordx4 v[62:65], v212, s[38:39] sc0 sc1 nt
	v_add_u32_e32 v213, 20, v214
	v_min_i32_e32 v213, s40, v213
	v_lshl_add_u32 v213, v213, 12, v211
	global_load_dwordx4 v[50:53], v213, s[38:39] sc0 sc1 nt
	v_add_u32_e32 v212, 24, v214
	v_min_i32_e32 v212, s40, v212
	v_lshl_add_u32 v212, v212, 12, v211
	global_load_dwordx4 v[54:57], v212, s[38:39] sc0 sc1 nt
	v_add_u32_e32 v213, 28, v214
	v_min_i32_e32 v213, s40, v213
	v_lshl_add_u32 v213, v213, 12, v211
	global_load_dwordx4 v[178:181], v213, s[38:39] sc0 sc1 nt
	s_lshr_b32 s4, s2, 4
	s_lshl_b32 s79, s6, 12
	s_lshl_b32 s84, s6, 13
	v_mov_b32_e32 v2, v3
	v_mov_b32_e32 v4, v3
	v_mov_b32_e32 v5, v3
	v_mov_b32_e32 v6, v3
	v_mov_b32_e32 v7, v3
	v_mov_b32_e32 v8, v3
	v_mov_b32_e32 v9, v3
	v_mov_b32_e32 v10, v3
	v_mov_b32_e32 v11, v3
	v_mov_b32_e32 v12, v3
	v_mov_b32_e32 v13, v3
	v_mov_b32_e32 v14, v3
	v_mov_b32_e32 v15, v3
	v_add_u32_e32 v1, 0x22100, v18
	v_mov_b64_e32 v[48:49], v[16:17]
	v_mov_b64_e32 v[32:33], v[16:17]
	v_and_b32_e32 v229, 63, v0
	s_lshl_b32 s33, s6, 5
	v_cmp_gt_u32_e64 s[0:1], 8, v0
	s_and_b32 s67, s4, 0xfff8
	s_add_i32 s84, s84, 0x12100
	s_mov_b32 s85, 0
	v_mov_b32_e32 v228, 1.0
	s_movk_i32 s86, 0x1040
	s_mov_b32 s78, 0x3e38aa3b
	v_mov_b32_e32 v235, 0x22110
	v_add_u32_e32 v236, s79, v230
	v_add_u32_e32 v237, s79, v231
	v_add_u32_e32 v238, s79, v232
	v_add_u32_e32 v239, s79, v233
	s_mov_b32 s87, 0x41000000
	v_mov_b32_e32 v240, 15
	v_mov_b32_e32 v241, 4
	v_mov_b32_e32 v242, 0xff800000
	v_lshrrev_b32_e32 v252, 4, v0
	v_and_b32_e32 v253, 15, v0
	v_lshlrev_b32_e32 v245, 12, v252
	v_lshl_or_b32 v245, v253, 4, v245
	v_add_u32_e32 v246, 0x20000, v245
	v_lshrrev_b32_e32 v254, 1, v253
	v_bfe_u32 v249, v252, 1, 3
	v_xor_b32_e32 v249, v254, v249
	v_lshlrev_b32_e32 v249, 4, v249
	v_lshl_add_u32 v249, v252, 7, v249
	v_and_b32_e32 v254, 1, v253
	v_lshl_add_u32 v249, v254, 3, v249
	v_lshrrev_b32_e32 v254, 3, v253
	v_mul_u32_u24_e32 v251, 0x1040, v254
	v_lshl_add_u32 v251, v252, 6, v251
	v_and_b32_e32 v254, 7, v253
	v_lshl_add_u32 v251, v254, 3, v251
	v_add_u32_e32 v250, 0x80, v251
	v_mov_b64_e32 v[46:47], v[14:15]
	v_mov_b64_e32 v[44:45], v[12:13]
	v_mov_b64_e32 v[42:43], v[10:11]
	v_mov_b64_e32 v[40:41], v[8:9]
	v_mov_b64_e32 v[38:39], v[6:7]
	v_mov_b64_e32 v[36:37], v[4:5]
	v_mov_b64_e32 v[34:35], v[2:3]
	v_mov_b64_e32 v[30:31], v[14:15]
	v_mov_b64_e32 v[28:29], v[12:13]
	v_mov_b64_e32 v[26:27], v[10:11]
	v_mov_b64_e32 v[24:25], v[8:9]
	v_mov_b64_e32 v[22:23], v[6:7]
	v_mov_b64_e32 v[20:21], v[4:5]
	v_mov_b64_e32 v[18:19], v[2:3]
	s_mov_b32 s11, 0
	s_mov_b32 s13, 0
	s_mov_b32 s14, 0
	s_mov_b32 s12, 0
	s_mov_b32 s10, 0
	s_branch .LBB0_7

.LBB0_7:
	s_add_i32 s95, s82, -1
	s_lshl_b32 s90, s91, 6
	s_add_i32 s96, s3, -1
	s_add_i32 s88, s89, s33
.Litem_loaded:
	s_cmp_eq_u32 s85, 0
	s_cselect_b64 s[4:5], -1, 0
	s_and_b64 s[8:9], s[4:5], s[0:1]
	s_and_saveexec_b64 s[6:7], s[8:9]
	s_cbranch_execz .LBB0_11
	s_movk_i32 s8, 0xff
	v_mov_b32_e32 v102, 0
	v_mov_b32_e32 v103, 0
	v_mov_b32_e32 v104, 0
	v_mov_b32_e32 v105, 0
	s_waitcnt vmcnt(16)
	v_mov_b32_e32 v2, v162
	v_cmp_ne_u16_e32 vcc, s8, v2
	s_and_saveexec_b64 s[8:9], vcc
	s_cbranch_execz .LBB0_10
	v_and_b32_sdwa v16, v2, v240 dst_sel:DWORD dst_unused:UNUSED_PAD src0_sel:WORD_0 src1_sel:DWORD
	v_readlane_b32 s16, v255, 0
	v_lshlrev_b32_e32 v16, 2, v16
	v_readlane_b32 s17, v255, 1
	s_nop 4
	global_load_dwordx2 v[102:103], v16, s[16:17]
	v_add_u32_sdwa v16, s2, v2 dst_sel:DWORD dst_unused:UNUSED_PAD src0_sel:DWORD src1_sel:WORD_0
	v_lshlrev_b32_sdwa v2, v241, v2 dst_sel:DWORD dst_unused:UNUSED_PAD src0_sel:DWORD src1_sel:WORD_0
	v_and_or_b32 v16, v16, 7, s67
	v_and_b32_e32 v2, 0xf00, v2
	v_lshl_or_b32 v104, v16, 16, v2
	s_waitcnt vmcnt(0)
	v_sub_u32_e32 v103, v103, v102
	v_add_u32_e32 v2, 63, v103
	v_ashrrev_i32_e32 v16, 31, v2
	v_lshrrev_b32_e32 v16, 26, v16
	v_add_u32_e32 v2, v2, v16
	v_ashrrev_i32_e32 v105, 6, v2
